# mLSTM chunk: the two 8-step LDS->MFMA loops software-pipelined with counted waits; post-loop reads batched
# speedup vs baseline: 1.0405x; 1.0050x over previous
; #define LAS __attribute__((address_space(3)))
; __device__ __forceinline__ void mlstm_unit(LAS unsigned char* lds, const bf16_t* __restrict__ PM, const float* __restrict__ GATES, bf16_t* __restrict__ Hout,
;                                            int b, int h, int dir, int vs, Conv& cvs, const int wave_) {
;     ...
;             for (int ks = 0; ks < 8; ++ks) {
;                 const bf16x8 A = *(const LAS bf16x8*)(lds + KS + (s0 + i16) * RQ + (32 * ks + 8 * g) * 2);
; #pragma unroll
;                 for (int tb = 0; tb < 2; ++tb) {
;                     const bf16x8 B = *(const LAS bf16x8*)(lds + QS + (16 * (tb0 + tb) + i16) * RQ + (32 * ks + 8 * g) * 2);
;                     accS[tb] = __builtin_amdgcn_mfma_f32_16x16x32_bf16(A, B, accS[tb], 0, 0, 0);
;                 }
;             }
; #pragma unroll
;             for (int tb = 0; tb < 2; ++tb) {
;                 const int tp = 16 * (tb0 + tb) + i16;
;                 const float Mt = *(LAS float*)(lds + SC_M + tp * 4);
;                 float v[4];
; #pragma unroll
;                 for (int r = 0; r < 4; ++r) {
;                     const int sp = s0 + 4 * g + r;
;                     const bool ok = dir ? (sp >= tp) : (sp <= tp);
;                     const float as = *(LAS float*)(lds + SC_A + sp * 4);
;                     v[r] = ok ? accS[tb][r] * __expf(as - Mt) : 0.f;
.LBB0_574:
	v_cndmask_b32_e64 v132, 0, 1, s[94:95]
	v_cmp_ne_u32_e64 s[30:31], 1, v132
	s_andn2_b64 vcc, exec, s[94:95]
	s_cbranch_vccnz .LBB0_594
	v_mov_b32_e32 v132, 0
	s_mov_b32 s2, 0
	v_mov_b32_e32 v133, v132
	v_mov_b32_e32 v134, v132
	v_mov_b32_e32 v135, v132
	v_mov_b32_e32 v136, v132
	v_mov_b32_e32 v137, v132
	v_mov_b32_e32 v138, v132
	v_mov_b32_e32 v139, v132
	ds_read_b128 v[202:205], v174
	ds_read_b128 v[206:209], v176
	ds_read_b128 v[210:213], v175
	ds_read_b128 v[214:217], v174 offset:64
	ds_read_b128 v[218:221], v176 offset:64
	ds_read_b128 v[222:225], v175 offset:64
	ds_read_b128 v[226:229], v174 offset:128
	ds_read_b128 v[230:233], v176 offset:128
	ds_read_b128 v[234:237], v175 offset:128
	ds_read_b128 v[238:241], v174 offset:192
	ds_read_b128 v[242:245], v176 offset:192
	ds_read_b128 v[246:249], v175 offset:192
	s_waitcnt lgkmcnt(9)
	v_mfma_f32_16x16x32_bf16 v[136:139], v[202:205], v[206:209], v[136:139]
	v_mfma_f32_16x16x32_bf16 v[132:135], v[202:205], v[210:213], v[132:135]
	ds_read_b128 v[202:205], v174 offset:256
	ds_read_b128 v[206:209], v176 offset:256
	ds_read_b128 v[210:213], v175 offset:256
	s_waitcnt lgkmcnt(9)
	v_mfma_f32_16x16x32_bf16 v[136:139], v[214:217], v[218:221], v[136:139]
	v_mfma_f32_16x16x32_bf16 v[132:135], v[214:217], v[222:225], v[132:135]
	ds_read_b128 v[214:217], v174 offset:320
	ds_read_b128 v[218:221], v176 offset:320
	ds_read_b128 v[222:225], v175 offset:320
	s_waitcnt lgkmcnt(9)
	v_mfma_f32_16x16x32_bf16 v[136:139], v[226:229], v[230:233], v[136:139]
	v_mfma_f32_16x16x32_bf16 v[132:135], v[226:229], v[234:237], v[132:135]
	ds_read_b128 v[226:229], v174 offset:384
	ds_read_b128 v[230:233], v176 offset:384
	ds_read_b128 v[234:237], v175 offset:384
	s_waitcnt lgkmcnt(9)
	v_mfma_f32_16x16x32_bf16 v[136:139], v[238:241], v[242:245], v[136:139]
	v_mfma_f32_16x16x32_bf16 v[132:135], v[238:241], v[246:249], v[132:135]
	ds_read_b128 v[238:241], v174 offset:448
	ds_read_b128 v[242:245], v176 offset:448
	ds_read_b128 v[246:249], v175 offset:448
	s_waitcnt lgkmcnt(9)
	v_mfma_f32_16x16x32_bf16 v[136:139], v[202:205], v[206:209], v[136:139]
	v_mfma_f32_16x16x32_bf16 v[132:135], v[202:205], v[210:213], v[132:135]
	s_waitcnt lgkmcnt(6)
	v_mfma_f32_16x16x32_bf16 v[136:139], v[214:217], v[218:221], v[136:139]
	v_mfma_f32_16x16x32_bf16 v[132:135], v[214:217], v[222:225], v[132:135]
	s_waitcnt lgkmcnt(3)
	v_mfma_f32_16x16x32_bf16 v[136:139], v[226:229], v[230:233], v[136:139]
	v_mfma_f32_16x16x32_bf16 v[132:135], v[226:229], v[234:237], v[132:135]
	s_waitcnt lgkmcnt(0)
	v_mfma_f32_16x16x32_bf16 v[136:139], v[238:241], v[242:245], v[136:139]
	v_mfma_f32_16x16x32_bf16 v[132:135], v[238:241], v[246:249], v[132:135]
	v_add_u32_e32 v152, 0, v167
	v_add_u32_e32 v152, 0x1fd00, v152
	ds_read_b32 v203, v152
	v_mov_b32_e32 v202, 0
	v_add_u32_e32 v152, 0x1fc00, v197
	v_mov_b32_e32 v204, 0
	s_and_saveexec_b64 s[2:3], s[14:15]
	s_cbranch_execz .LBB0_579
	ds_read_b32 v204, v152
	s_waitcnt lgkmcnt(0)
	v_sub_f32_e32 v204, v204, v203
	v_mul_f32_e32 v204, 0x3fb8aa3b, v204
	v_exp_f32_e32 v204, v204
	s_nop 0
	v_mul_f32_e32 v204, v136, v204

; #define LAS __attribute__((address_space(3)))
; __device__ __forceinline__ void mlstm_unit(LAS unsigned char* lds, const bf16_t* __restrict__ PM, const float* __restrict__ GATES, bf16_t* __restrict__ Hout,
;                                            int b, int h, int dir, int vs, Conv& cvs, const int wave_) {
;     ...
; #pragma unroll 2
;             for (int ks = 0; ks < 8; ++ks) {
;                 const bf16x8 A = *(const LAS bf16x8*)(lds + CTS + (v0 + i16) * RQ + (32 * ks + 8 * g) * 2);
; #pragma unroll
;                 for (int tb = 0; tb < 2; ++tb) {
;                     const bf16x8 B = *(const LAS bf16x8*)(lds + QS + (16 * (tb0 + tb) + i16) * RQ + (32 * ks + 8 * g) * 2);
;                     accO[tb] = __builtin_amdgcn_mfma_f32_16x16x32_bf16(A, B, accO[tb], 0, 0, 0);
;                 }
;             }
; #pragma unroll
;             for (int tb = 0; tb < 2; ++tb) accO[tb] *= *(LAS float*)(lds + SC_WI + (16 * (tb0 + tb) + i16) * 4);
; #pragma unroll
;             for (int s2 = 0; s2 < 2; ++s2) {
;                 const bf16x8 A = tr_pair(lds + VS + (32 * s2 + 8 * g + q4) * RV + (v0 + 4 * p4) * 2, 4 * RV);
; #pragma unroll
;                 for (int tb = 0; tb < 2; ++tb) {
;                     const bf16x8 B = *(const LAS bf16x8*)(lds + SS + (16 * (tb0 + tb) + i16) * RV + (32 * s2 + 8 * g) * 2);
;                     accO[tb] = __builtin_amdgcn_mfma_f32_16x16x32_bf16(A, B, accO[tb], 0, 0, 0);
;                 }
;             }
.LBB0_597:
	s_or_b64 exec, exec, s[2:3]
	v_mov_b32_e32 v132, 0
	s_mov_b32 s2, 0
	v_mov_b32_e32 v133, v132
	v_mov_b32_e32 v134, v132
	v_mov_b32_e32 v135, v132
	v_mov_b32_e32 v136, v132
	v_mov_b32_e32 v137, v132
	v_mov_b32_e32 v138, v132
	v_mov_b32_e32 v139, v132
	v_add_u32_e32 v152, 0x17400, v178
	ds_read_b128 v[202:205], v152
	ds_read_b128 v[206:209], v176
	ds_read_b128 v[210:213], v177
	ds_read_b128 v[214:217], v152 offset:64
	ds_read_b128 v[218:221], v176 offset:64
	ds_read_b128 v[222:225], v177 offset:64
	ds_read_b128 v[226:229], v152 offset:128
	ds_read_b128 v[230:233], v176 offset:128
	ds_read_b128 v[234:237], v177 offset:128
	ds_read_b128 v[238:241], v152 offset:192
	ds_read_b128 v[242:245], v176 offset:192
	ds_read_b128 v[246:249], v177 offset:192
	s_waitcnt lgkmcnt(9)
	v_mfma_f32_16x16x32_bf16 v[136:139], v[202:205], v[206:209], v[136:139]
	v_mfma_f32_16x16x32_bf16 v[132:135], v[202:205], v[210:213], v[132:135]
	ds_read_b128 v[202:205], v152 offset:256
	ds_read_b128 v[206:209], v176 offset:256
	ds_read_b128 v[210:213], v177 offset:256
	s_waitcnt lgkmcnt(9)
	v_mfma_f32_16x16x32_bf16 v[136:139], v[214:217], v[218:221], v[136:139]
	v_mfma_f32_16x16x32_bf16 v[132:135], v[214:217], v[222:225], v[132:135]
	ds_read_b128 v[214:217], v152 offset:320
	ds_read_b128 v[218:221], v176 offset:320
	ds_read_b128 v[222:225], v177 offset:320
	s_waitcnt lgkmcnt(9)
	v_mfma_f32_16x16x32_bf16 v[136:139], v[226:229], v[230:233], v[136:139]
	v_mfma_f32_16x16x32_bf16 v[132:135], v[226:229], v[234:237], v[132:135]
	ds_read_b128 v[226:229], v152 offset:384
	ds_read_b128 v[230:233], v176 offset:384
	ds_read_b128 v[234:237], v177 offset:384
	s_waitcnt lgkmcnt(9)
	v_mfma_f32_16x16x32_bf16 v[136:139], v[238:241], v[242:245], v[136:139]
	v_mfma_f32_16x16x32_bf16 v[132:135], v[238:241], v[246:249], v[132:135]
	ds_read_b128 v[238:241], v152 offset:448
	ds_read_b128 v[242:245], v176 offset:448
	ds_read_b128 v[246:249], v177 offset:448
	s_waitcnt lgkmcnt(9)
	v_mfma_f32_16x16x32_bf16 v[136:139], v[202:205], v[206:209], v[136:139]
	v_mfma_f32_16x16x32_bf16 v[132:135], v[202:205], v[210:213], v[132:135]
	s_waitcnt lgkmcnt(6)
	v_mfma_f32_16x16x32_bf16 v[136:139], v[214:217], v[218:221], v[136:139]
	v_mfma_f32_16x16x32_bf16 v[132:135], v[214:217], v[222:225], v[132:135]
	s_waitcnt lgkmcnt(3)
	v_mfma_f32_16x16x32_bf16 v[136:139], v[226:229], v[230:233], v[136:139]
	v_mfma_f32_16x16x32_bf16 v[132:135], v[226:229], v[234:237], v[132:135]
	s_waitcnt lgkmcnt(0)
	v_mfma_f32_16x16x32_bf16 v[136:139], v[238:241], v[242:245], v[136:139]
	v_mfma_f32_16x16x32_bf16 v[132:135], v[238:241], v[246:249], v[132:135]
	v_add_u32_e32 v230, s63, v162
	v_add_u32_e32 v231, s56, v162
	v_add_u32_e32 v232, v163, v169
	v_add_u32_e32 v233, v170, v168
	v_add_u32_e32 v234, v170, v173
	v_add_u32_e32 v235, v171, v168
	v_add_u32_e32 v236, v171, v173
	ds_read_b32 v226, v230
	ds_read_b32 v228, v231
	ds_read_b64_tr_b16 v[202:203], v232
	ds_read_b64_tr_b16 v[204:205], v232 offset:576
	ds_read_b128 v[206:209], v233
	ds_read_b128 v[210:213], v234
	ds_read_b64_tr_b16 v[214:215], v190
	ds_read_b64_tr_b16 v[216:217], v190 offset:576
	ds_read_b128 v[218:221], v235
	ds_read_b128 v[222:225], v236
	s_waitcnt lgkmcnt(8)
	v_pk_mul_f32 v[138:139], v[138:139], v[226:227] op_sel_hi:[1,0]
	v_pk_mul_f32 v[136:137], v[136:137], v[226:227] op_sel_hi:[1,0]
	v_pk_mul_f32 v[134:135], v[134:135], v[228:229] op_sel_hi:[1,0]
	v_pk_mul_f32 v[132:133], v[132:133], v[228:229] op_sel_hi:[1,0]
	s_waitcnt lgkmcnt(4)
	s_nop 1
	v_mfma_f32_16x16x32_bf16 v[136:139], v[202:205], v[206:209], v[136:139]
	v_mfma_f32_16x16x32_bf16 v[132:135], v[202:205], v[210:213], v[132:135]
	s_waitcnt lgkmcnt(0)
	v_mfma_f32_16x16x32_bf16 v[136:139], v[214:217], v[218:221], v[136:139]
	v_mfma_f32_16x16x32_bf16 v[132:135], v[214:217], v[222:225], v[132:135]
